# MoE gate/up unit loop: expert of the row tile carried in registers (looked up once, asynchronously, one unit ahead) instead of two dependent lookups with full vmcnt drains per unit
# speedup vs baseline: 1.0018x; 1.0018x over previous
.LBB0_2632:
	s_add_u32 s50, s86, 0xd00000
	s_addc_u32 s51, s87, 0
	s_add_u32 s52, s86, 0x13400000
	s_addc_u32 s53, s87, 0
	s_add_i32 s0, s5, s0
	s_mul_hi_i32 s1, s0, 0x2e8ba2e9
	s_lshr_b32 s5, s1, 31
	s_ashr_i32 s1, s1, 5
	s_add_i32 s1, s1, s5
	s_lshl_b32 s8, s1, 2
	s_sub_i32 s5, s27, s8
	s_min_i32 s9, s5, 4
	s_abs_i32 s10, s9
	v_cvt_f32_u32_e32 v1, s10
	s_sub_i32 s13, 0, s10
	s_mulk_i32 s1, 0xb0
	s_sub_i32 s0, s0, s1
	v_rcp_iflag_f32_e32 v1, v1
	s_abs_i32 s12, s0
	s_lshr_b32 s5, s4, 6
	s_xor_b32 s1, s0, s9
	v_mul_f32_e32 v1, 0x4f7ffffe, v1
	v_cvt_u32_f32_e32 v1, v1
	s_lshr_b32 s11, s4, 8
	s_lshl_b32 s54, s5, 10
	s_ashr_i32 s1, s1, 31
	v_readfirstlane_b32 s14, v1
	s_mul_i32 s13, s13, s14
	s_mul_hi_u32 s13, s14, s13
	s_add_i32 s14, s14, s13
	s_mul_hi_u32 s13, s12, s14
	s_mul_i32 s14, s13, s10
	s_sub_i32 s12, s12, s14
	s_add_i32 s14, s13, 1
	s_sub_i32 s15, s12, s10
	s_cmp_ge_u32 s12, s10
	s_cselect_b32 s13, s14, s13
	s_cselect_b32 s12, s15, s12
	s_add_i32 s14, s13, 1
	s_cmp_ge_u32 s12, s10
	s_cselect_b32 s10, s14, s13
	s_xor_b32 s10, s10, s1
	s_sub_i32 s38, s10, s1
	s_mul_i32 s1, s38, s9
	s_sub_i32 s0, s0, s1
	s_add_i32 s40, s8, s0
	s_ashr_i32 s41, s40, 31
	s_lshl_b64 s[0:1], s[40:41], 19
	s_lshl_b64 s[8:9], s[40:41], 2
	s_add_u32 s8, s33, s8
	v_mov_b32_e32 v147, 0
	s_addc_u32 s9, s48, s9
	global_load_dword v1, v147, s[8:9]
	v_lshlrev_b32_e32 v2, 4, v0
	v_and_b32_e32 v3, 32, v0
	v_lshrrev_b32_e32 v4, 1, v0
	v_lshrrev_b32_e32 v5, 5, v0
	v_bfe_u32 v6, v0, 2, 2
	v_bitop3_b32 v14, v2, v3, 48 bitop3:0x6c
	v_and_b32_e32 v16, 24, v4
	v_and_b32_e32 v3, 4, v5
	v_or_b32_e32 v15, 0x2000, v2
	v_bfe_u32 v13, v0, 2, 4
	v_and_b32_e32 v12, 64, v0
	v_lshrrev_b32_e32 v7, 3, v0
	s_movk_i32 s12, 0x60
	v_or3_b32 v3, v3, v6, v16
	v_lshrrev_b32_e32 v5, 7, v15
	s_ashr_i32 s39, s38, 31
	s_movk_i32 s10, 0x70
	v_and_or_b32 v4, v7, 48, v13
	v_or_b32_e32 v2, v14, v12
	v_and_or_b32 v6, v7, 32, v3
	v_and_or_b32 v3, v5, s12, v3
	s_lshl_b64 s[12:13], s[38:39], 19
	s_mov_b32 s55, 0x1600000
	v_lshl_or_b32 v148, v4, 11, v2
	v_and_or_b32 v4, v5, s10, v13
	s_add_u32 s12, s52, s12
	v_lshl_or_b32 v146, v6, 11, v2
	v_lshl_or_b32 v150, v4, 11, v2
	v_lshl_or_b32 v152, v3, 11, v2
	s_addc_u32 s13, s53, s13
	s_add_i32 s39, s54, 0
	s_mov_b64 s[8:9], 0x40000
	s_add_i32 m0, s39, 0x10000
	v_mov_b32_e32 v153, v147
	v_mov_b32_e32 v149, v147
	v_mov_b32_e32 v151, v147
	s_mov_b32 s10, 0
	s_waitcnt vmcnt(0)
	v_readfirstlane_b32 s100, v1
	v_mul_hi_i32 v3, v1, s55
	v_mul_lo_u32 v2, v1, s55
	v_lshl_add_u64 v[2:3], s[12:13], 0, v[2:3]
	v_lshl_add_u64 v[4:5], v[2:3], 0, s[8:9]
	v_readfirstlane_b32 s12, v2
	v_readfirstlane_b32 s13, v3
	v_readfirstlane_b32 s14, v4
	v_readfirstlane_b32 s15, v5
	v_lshl_add_u64 v[10:11], v[2:3], 0, v[146:147]
	v_lshl_add_u64 v[8:9], v[2:3], 0, v[152:153]
	s_nop 0
	global_load_lds_dwordx4 v146, s[12:13]
	s_add_i32 m0, s39, 0x12000
	s_nop 0
	global_load_lds_dwordx4 v152, s[12:13]
	s_add_i32 m0, s39, 0x14000
	s_nop 0
	global_load_lds_dwordx4 v146, s[14:15]
	s_add_i32 m0, s39, 0x16000
	s_add_u32 s42, s50, s0
	s_addc_u32 s43, s51, s1
	s_add_i32 s56, s39, 0x2000
	global_load_lds_dwordx4 v152, s[14:15]
	s_mov_b32 m0, s39
	s_add_u32 s0, s42, 0x40000
	global_load_lds_dwordx4 v148, s[42:43]
	s_mov_b32 m0, s56
	s_addc_u32 s1, s43, 0
	s_add_i32 s57, s39, 0x4000
	global_load_lds_dwordx4 v150, s[42:43]
	s_add_i32 s58, s39, 0x6000
	s_mov_b32 m0, s57
	s_cmp_eq_u32 s11, 1
	global_load_lds_dwordx4 v148, s[0:1]
	s_mov_b32 m0, s58
	v_lshl_add_u64 v[4:5], s[42:43], 0, v[148:149]
	global_load_lds_dwordx4 v150, s[0:1]
	s_cselect_b64 s[12:13], -1, 0
	s_cmp_lg_u32 s11, 1
	v_lshl_add_u64 v[6:7], s[42:43], 0, v[150:151]
	s_cbranch_scc1 .LBB0_2634
	s_barrier

.LBB0_2636:
	s_andn2_b64 vcc, exec, s[0:1]
	s_mov_b32 s38, s30
	s_mov_b32 s40, s34
	v_mov_b64_e32 v[2:3], v[182:183]
	s_mov_b32 s100, s101
	s_mov_b64 s[42:43], s[36:37]
	s_cbranch_vccz .LBB0_2656

.LBB0_2646:
	s_nop 0
	v_cndmask_b32_e64 v4, 0, 1, s[4:5]
	s_ashr_i32 s35, s34, 31
	v_cmp_ne_u32_e64 s[0:1], 1, v4
	s_andn2_b64 vcc, exec, s[4:5]
	v_mov_b64_e32 v[182:183], v[2:3]
	v_readfirstlane_b32 s98, v2
	v_readfirstlane_b32 s99, v3
	v_mov_b32_e32 v255, 0
	s_cbranch_vccnz .LBB0_2648
	s_lshl_b64 s[36:37], s[34:35], 2
	s_add_u32 s36, s33, s36
	s_addc_u32 s37, s48, s37
	global_load_dword v255, v147, s[36:37]
	s_ashr_i32 s31, s30, 31
	s_lshl_b64 s[36:37], s[30:31], 19
	s_add_u32 s98, s52, s36
	s_addc_u32 s99, s53, s37

.LBB0_2649:
	ds_read_b128 v[96:99], v163
	ds_read_b128 v[106:109], v163 offset:1024
	ds_read_b128 v[110:113], v163 offset:2048
	ds_read_b128 v[188:191], v163 offset:3072
	ds_read_b128 v[192:195], v185
	ds_read_b128 v[196:199], v185 offset:1024
	ds_read_b128 v[200:203], v185 offset:2048
	ds_read_b128 v[204:207], v185 offset:3072
	s_add_u32 s35, s4, 0xfffc0080
	s_addc_u32 s41, s5, -1
	s_cmp_eq_u32 s31, 12
	s_cselect_b64 vcc, -1, 0
	s_cselect_b32 s43, s11, s41
	s_cselect_b32 s42, s29, s35
	v_cndmask_b32_e32 v241, v95, v183, vcc
	v_cndmask_b32_e32 v240, v94, v182, vcc
	v_lshl_add_u64 v[100:101], s[4:5], 0, v[176:177]
	s_add_i32 m0, s39, 0xc000
	ds_read_b128 v[208:211], v155
	ds_read_b128 v[212:215], v155 offset:1024
	ds_read_b128 v[216:219], v155 offset:2048
	ds_read_b128 v[220:223], v155 offset:3072
	ds_read_b128 v[224:227], v155 offset:4096
	ds_read_b128 v[228:231], v155 offset:5120
	ds_read_b128 v[232:235], v155 offset:6144
	ds_read_b128 v[236:239], v155 offset:7168
	global_load_lds_dwordx4 v[100:101], off
	v_lshl_add_u64 v[100:101], s[4:5], 0, v[178:179]
	s_add_i32 m0, s39, 0xe000
	s_nop 0
	global_load_lds_dwordx4 v[100:101], off
	s_waitcnt vmcnt(8)
	v_mul_lo_u32 v182, v255, s55
	v_mov_b32_e32 v183, 0
	s_nop 0
	v_lshl_add_u64 v[182:183], v[182:183], 0, s[98:99]
	s_waitcnt lgkmcnt(0)
	s_barrier
	s_setprio 1
	s_waitcnt lgkmcnt(0)
	v_mfma_i32_16x16x64_i8 v[142:145], v[96:99], v[208:211], v[142:145]
	v_mfma_i32_16x16x64_i8 v[134:137], v[110:113], v[208:211], v[134:137]
	v_mfma_i32_16x16x64_i8 v[126:129], v[96:99], v[216:219], v[126:129]
	v_mfma_i32_16x16x64_i8 v[118:121], v[110:113], v[216:219], v[118:121]
	v_mfma_i32_16x16x64_i8 v[100:103], v[96:99], v[224:227], v[102:105]
	v_mfma_i32_16x16x64_i8 v[86:89], v[110:113], v[224:227], v[86:89]
	v_mfma_i32_16x16x64_i8 v[78:81], v[96:99], v[232:235], v[78:81]
	v_mfma_i32_16x16x64_i8 v[70:73], v[110:113], v[232:235], v[70:73]
	v_mfma_i32_16x16x64_i8 v[142:145], v[106:109], v[212:215], v[142:145]
	v_mfma_i32_16x16x64_i8 v[134:137], v[188:191], v[212:215], v[134:137]
	v_mfma_i32_16x16x64_i8 v[126:129], v[106:109], v[220:223], v[126:129]
	v_mfma_i32_16x16x64_i8 v[118:121], v[188:191], v[220:223], v[118:121]
	v_mfma_i32_16x16x64_i8 v[100:103], v[106:109], v[228:231], v[100:103]
	v_mfma_i32_16x16x64_i8 v[86:89], v[188:191], v[228:231], v[86:89]
	v_mfma_i32_16x16x64_i8 v[78:81], v[106:109], v[236:239], v[78:81]
	v_mfma_i32_16x16x64_i8 v[70:73], v[188:191], v[236:239], v[70:73]
	s_setprio 0
	s_setprio 1
	v_mfma_i32_16x16x64_i8 v[138:141], v[192:195], v[208:211], v[138:141]
	v_mfma_i32_16x16x64_i8 v[130:133], v[200:203], v[208:211], v[130:133]
	v_mfma_i32_16x16x64_i8 v[122:125], v[192:195], v[216:219], v[122:125]
	v_mfma_i32_16x16x64_i8 v[114:117], v[200:203], v[216:219], v[114:117]
	v_mfma_i32_16x16x64_i8 v[90:93], v[192:195], v[224:227], v[90:93]
	v_mfma_i32_16x16x64_i8 v[82:85], v[200:203], v[224:227], v[82:85]
	v_mfma_i32_16x16x64_i8 v[74:77], v[192:195], v[232:235], v[74:77]
	v_mfma_i32_16x16x64_i8 v[66:69], v[200:203], v[232:235], v[66:69]
	v_mfma_i32_16x16x64_i8 v[138:141], v[196:199], v[212:215], v[138:141]
	v_mfma_i32_16x16x64_i8 v[130:133], v[204:207], v[212:215], v[130:133]
	v_mfma_i32_16x16x64_i8 v[122:125], v[196:199], v[220:223], v[122:125]
	v_mfma_i32_16x16x64_i8 v[114:117], v[204:207], v[220:223], v[114:117]
	v_mfma_i32_16x16x64_i8 v[90:93], v[196:199], v[228:231], v[90:93]
	v_mfma_i32_16x16x64_i8 v[82:85], v[204:207], v[228:231], v[82:85]
	v_mfma_i32_16x16x64_i8 v[74:77], v[196:199], v[236:239], v[74:77]
	v_mfma_i32_16x16x64_i8 v[66:69], v[204:207], v[236:239], v[66:69]
	s_setprio 0
	s_barrier
	s_add_i32 s35, s62, s54
	v_lshl_add_u64 v[242:243], v[240:241], 0, v[146:147]
	s_mov_b32 m0, s35
	ds_read_b128 v[208:211], v155 offset:16384
	ds_read_b128 v[212:215], v155 offset:17408
	ds_read_b128 v[216:219], v155 offset:18432
	ds_read_b128 v[220:223], v155 offset:19456
	ds_read_b128 v[224:227], v155 offset:20480
	ds_read_b128 v[228:231], v155 offset:21504
	ds_read_b128 v[232:235], v155 offset:22528
	ds_read_b128 v[236:239], v155 offset:23552
	global_load_lds_dwordx4 v[242:243], off
	v_lshl_add_u64 v[244:245], v[240:241], 0, v[152:153]
	s_add_i32 m0, s35, 0x2000
	v_lshl_add_u64 v[104:105], v[240:241], 0, s[8:9]
	s_add_i32 s35, s63, s54
	global_load_lds_dwordx4 v[244:245], off
	v_lshl_add_u64 v[246:247], v[104:105], 0, v[146:147]
	s_mov_b32 m0, s35
	v_lshl_add_u64 v[104:105], v[104:105], 0, v[152:153]
	global_load_lds_dwordx4 v[246:247], off
	s_add_i32 m0, s35, 0x2000
	v_lshl_add_u64 v[246:247], s[42:43], 0, v[148:149]
	global_load_lds_dwordx4 v[104:105], off
	s_mov_b32 m0, s39
	v_lshl_add_u64 v[248:249], s[42:43], 0, v[150:151]
	global_load_lds_dwordx4 v[246:247], off
	s_mov_b32 m0, s56
	s_nop 0
	global_load_lds_dwordx4 v[248:249], off
	s_waitcnt vmcnt(8)
	s_waitcnt lgkmcnt(0)
	s_barrier
	s_setprio 1
	s_waitcnt lgkmcnt(0)
	v_mfma_i32_16x16x64_i8 v[62:65], v[96:99], v[208:211], v[62:65]
	v_mfma_i32_16x16x64_i8 v[54:57], v[110:113], v[208:211], v[54:57]
	v_mfma_i32_16x16x64_i8 v[46:49], v[96:99], v[216:219], v[46:49]
	v_mfma_i32_16x16x64_i8 v[38:41], v[110:113], v[216:219], v[38:41]
	v_mfma_i32_16x16x64_i8 v[30:33], v[96:99], v[224:227], v[30:33]
	v_mfma_i32_16x16x64_i8 v[22:25], v[110:113], v[224:227], v[22:25]
	v_mfma_i32_16x16x64_i8 v[14:17], v[96:99], v[232:235], v[14:17]
	v_mfma_i32_16x16x64_i8 v[6:9], v[110:113], v[232:235], v[6:9]
	v_mfma_i32_16x16x64_i8 v[62:65], v[106:109], v[212:215], v[62:65]
	v_mfma_i32_16x16x64_i8 v[54:57], v[188:191], v[212:215], v[54:57]
	v_mfma_i32_16x16x64_i8 v[46:49], v[106:109], v[220:223], v[46:49]
	v_mfma_i32_16x16x64_i8 v[38:41], v[188:191], v[220:223], v[38:41]
	v_mfma_i32_16x16x64_i8 v[30:33], v[106:109], v[228:231], v[30:33]
	v_mfma_i32_16x16x64_i8 v[22:25], v[188:191], v[228:231], v[22:25]
	v_mfma_i32_16x16x64_i8 v[14:17], v[106:109], v[236:239], v[14:17]
	v_mfma_i32_16x16x64_i8 v[6:9], v[188:191], v[236:239], v[6:9]
	s_setprio 0
	s_setprio 1
	v_mfma_i32_16x16x64_i8 v[58:61], v[192:195], v[208:211], v[58:61]
	v_mfma_i32_16x16x64_i8 v[50:53], v[200:203], v[208:211], v[50:53]
	v_mfma_i32_16x16x64_i8 v[42:45], v[192:195], v[216:219], v[42:45]
	v_mfma_i32_16x16x64_i8 v[34:37], v[200:203], v[216:219], v[34:37]
	v_mfma_i32_16x16x64_i8 v[26:29], v[192:195], v[224:227], v[26:29]
	v_mfma_i32_16x16x64_i8 v[18:21], v[200:203], v[224:227], v[18:21]
	v_mfma_i32_16x16x64_i8 v[10:13], v[192:195], v[232:235], v[10:13]
	v_mfma_i32_16x16x64_i8 v[2:5], v[200:203], v[232:235], v[2:5]
	v_mfma_i32_16x16x64_i8 v[58:61], v[196:199], v[212:215], v[58:61]
	v_mfma_i32_16x16x64_i8 v[50:53], v[204:207], v[212:215], v[50:53]
	v_mfma_i32_16x16x64_i8 v[42:45], v[196:199], v[220:223], v[42:45]
	v_mfma_i32_16x16x64_i8 v[34:37], v[204:207], v[220:223], v[34:37]
	v_mfma_i32_16x16x64_i8 v[26:29], v[196:199], v[228:231], v[26:29]
	v_mfma_i32_16x16x64_i8 v[18:21], v[204:207], v[228:231], v[18:21]
	v_mfma_i32_16x16x64_i8 v[10:13], v[196:199], v[236:239], v[10:13]
	v_mfma_i32_16x16x64_i8 v[2:5], v[204:207], v[236:239], v[2:5]
	s_setprio 0
	s_barrier
	s_add_i32 s35, 0, 0x18000
	v_add_u32_e32 v104, s35, v1
	s_add_i32 s41, 0, 0x1c000
	ds_read_b128 v[96:99], v104
	ds_read_b128 v[106:109], v104 offset:1024
	ds_read_b128 v[110:113], v104 offset:2048
	ds_read_b128 v[188:191], v104 offset:3072
	v_add_u32_e32 v104, s41, v1
	ds_read_b128 v[192:195], v104
	ds_read_b128 v[196:199], v104 offset:1024
	ds_read_b128 v[200:203], v104 offset:2048
	ds_read_b128 v[204:207], v104 offset:3072
	s_add_u32 s42, s42, 0x40000
	s_addc_u32 s43, s43, 0
	s_mov_b32 m0, s57
	v_lshl_add_u64 v[104:105], s[42:43], 0, v[148:149]
	ds_read_b128 v[208:211], v155 offset:32768
	ds_read_b128 v[212:215], v155 offset:33792
	ds_read_b128 v[216:219], v155 offset:34816
	ds_read_b128 v[220:223], v155 offset:35840
	ds_read_b128 v[224:227], v155 offset:36864
	ds_read_b128 v[228:231], v155 offset:37888
	ds_read_b128 v[232:235], v155 offset:38912
	ds_read_b128 v[236:239], v155 offset:39936
	global_load_lds_dwordx4 v[104:105], off
	v_lshl_add_u64 v[104:105], s[42:43], 0, v[150:151]
	s_mov_b32 m0, s58
	s_nop 0
	global_load_lds_dwordx4 v[104:105], off
	s_waitcnt vmcnt(8)
	s_waitcnt lgkmcnt(0)
	s_barrier
	s_setprio 1
	s_waitcnt lgkmcnt(0)
	v_mfma_i32_16x16x64_i8 v[142:145], v[96:99], v[208:211], v[142:145]
	v_mfma_i32_16x16x64_i8 v[134:137], v[110:113], v[208:211], v[134:137]
	v_mfma_i32_16x16x64_i8 v[126:129], v[96:99], v[216:219], v[126:129]
	v_mfma_i32_16x16x64_i8 v[118:121], v[110:113], v[216:219], v[118:121]
	v_mfma_i32_16x16x64_i8 v[100:103], v[96:99], v[224:227], v[100:103]
	v_mfma_i32_16x16x64_i8 v[86:89], v[110:113], v[224:227], v[86:89]
	v_mfma_i32_16x16x64_i8 v[78:81], v[96:99], v[232:235], v[78:81]
	v_mfma_i32_16x16x64_i8 v[70:73], v[110:113], v[232:235], v[70:73]
	v_mfma_i32_16x16x64_i8 v[142:145], v[106:109], v[212:215], v[142:145]
	v_mfma_i32_16x16x64_i8 v[134:137], v[188:191], v[212:215], v[134:137]
	v_mfma_i32_16x16x64_i8 v[126:129], v[106:109], v[220:223], v[126:129]
	v_mfma_i32_16x16x64_i8 v[118:121], v[188:191], v[220:223], v[118:121]
	v_mfma_i32_16x16x64_i8 v[102:105], v[106:109], v[228:231], v[100:103]
	v_mfma_i32_16x16x64_i8 v[86:89], v[188:191], v[228:231], v[86:89]
	v_mfma_i32_16x16x64_i8 v[78:81], v[106:109], v[236:239], v[78:81]
	v_mfma_i32_16x16x64_i8 v[70:73], v[188:191], v[236:239], v[70:73]
	s_setprio 0
	s_setprio 1
	v_mfma_i32_16x16x64_i8 v[138:141], v[192:195], v[208:211], v[138:141]
	v_mfma_i32_16x16x64_i8 v[130:133], v[200:203], v[208:211], v[130:133]
	v_mfma_i32_16x16x64_i8 v[122:125], v[192:195], v[216:219], v[122:125]
	v_mfma_i32_16x16x64_i8 v[114:117], v[200:203], v[216:219], v[114:117]
	v_mfma_i32_16x16x64_i8 v[90:93], v[192:195], v[224:227], v[90:93]
	v_mfma_i32_16x16x64_i8 v[82:85], v[200:203], v[224:227], v[82:85]
	v_mfma_i32_16x16x64_i8 v[74:77], v[192:195], v[232:235], v[74:77]
	v_mfma_i32_16x16x64_i8 v[66:69], v[200:203], v[232:235], v[66:69]
	v_mfma_i32_16x16x64_i8 v[138:141], v[196:199], v[212:215], v[138:141]
	v_mfma_i32_16x16x64_i8 v[130:133], v[204:207], v[212:215], v[130:133]
	v_mfma_i32_16x16x64_i8 v[122:125], v[196:199], v[220:223], v[122:125]
	v_mfma_i32_16x16x64_i8 v[114:117], v[204:207], v[220:223], v[114:117]
	v_mfma_i32_16x16x64_i8 v[90:93], v[196:199], v[228:231], v[90:93]
	v_mfma_i32_16x16x64_i8 v[82:85], v[204:207], v[228:231], v[82:85]
	v_mfma_i32_16x16x64_i8 v[74:77], v[196:199], v[236:239], v[74:77]
	v_mfma_i32_16x16x64_i8 v[66:69], v[204:207], v[236:239], v[66:69]
	s_setprio 0
	s_barrier
	s_add_i32 s35, s35, s54
	v_lshl_add_u64 v[100:101], v[242:243], 0, s[18:19]
	s_mov_b32 m0, s35
	ds_read_b128 v[208:211], v155 offset:49152
	ds_read_b128 v[212:215], v155 offset:50176
	ds_read_b128 v[216:219], v155 offset:51200
	ds_read_b128 v[220:223], v155 offset:52224
	ds_read_b128 v[224:227], v155 offset:53248
	ds_read_b128 v[228:231], v155 offset:54272
	ds_read_b128 v[232:235], v155 offset:55296
	ds_read_b128 v[236:239], v155 offset:56320
	global_load_lds_dwordx4 v[100:101], off
	v_lshl_add_u64 v[100:101], v[244:245], 0, s[18:19]
	s_add_i32 m0, s35, 0x2000
	s_add_i32 s35, s41, s54
	global_load_lds_dwordx4 v[100:101], off
	v_lshl_add_u64 v[100:101], v[240:241], 0, s[20:21]
	v_lshl_add_u64 v[240:241], v[100:101], 0, v[146:147]
	s_mov_b32 m0, s35
	v_lshl_add_u64 v[100:101], v[100:101], 0, v[152:153]
	global_load_lds_dwordx4 v[240:241], off
	s_add_i32 m0, s35, 0x2000
	s_nop 0
	global_load_lds_dwordx4 v[100:101], off
	v_lshl_add_u64 v[100:101], v[246:247], 0, s[18:19]
	s_mov_b32 m0, s59
	s_nop 0
	global_load_lds_dwordx4 v[100:101], off
	v_lshl_add_u64 v[100:101], v[248:249], 0, s[18:19]
	s_mov_b32 m0, s60
	s_nop 0
	global_load_lds_dwordx4 v[100:101], off
	s_waitcnt vmcnt(8)
	s_waitcnt lgkmcnt(0)
	s_barrier
	s_setprio 1
	s_waitcnt lgkmcnt(0)
	v_mfma_i32_16x16x64_i8 v[62:65], v[96:99], v[208:211], v[62:65]
	v_mfma_i32_16x16x64_i8 v[54:57], v[110:113], v[208:211], v[54:57]
	v_mfma_i32_16x16x64_i8 v[46:49], v[96:99], v[216:219], v[46:49]
	v_mfma_i32_16x16x64_i8 v[38:41], v[110:113], v[216:219], v[38:41]
	v_mfma_i32_16x16x64_i8 v[30:33], v[96:99], v[224:227], v[30:33]
	v_mfma_i32_16x16x64_i8 v[22:25], v[110:113], v[224:227], v[22:25]
	v_mfma_i32_16x16x64_i8 v[14:17], v[96:99], v[232:235], v[14:17]
	v_mfma_i32_16x16x64_i8 v[6:9], v[110:113], v[232:235], v[6:9]
	v_mfma_i32_16x16x64_i8 v[62:65], v[106:109], v[212:215], v[62:65]
	v_mfma_i32_16x16x64_i8 v[54:57], v[188:191], v[212:215], v[54:57]
	v_mfma_i32_16x16x64_i8 v[46:49], v[106:109], v[220:223], v[46:49]
	v_mfma_i32_16x16x64_i8 v[38:41], v[188:191], v[220:223], v[38:41]
	v_mfma_i32_16x16x64_i8 v[30:33], v[106:109], v[228:231], v[30:33]
	v_mfma_i32_16x16x64_i8 v[22:25], v[188:191], v[228:231], v[22:25]
	v_mfma_i32_16x16x64_i8 v[14:17], v[106:109], v[236:239], v[14:17]
	v_mfma_i32_16x16x64_i8 v[6:9], v[188:191], v[236:239], v[6:9]
	s_setprio 0
	s_setprio 1
	v_mfma_i32_16x16x64_i8 v[58:61], v[192:195], v[208:211], v[58:61]
	v_mfma_i32_16x16x64_i8 v[50:53], v[200:203], v[208:211], v[50:53]
	v_mfma_i32_16x16x64_i8 v[42:45], v[192:195], v[216:219], v[42:45]
	v_mfma_i32_16x16x64_i8 v[34:37], v[200:203], v[216:219], v[34:37]
	v_mfma_i32_16x16x64_i8 v[26:29], v[192:195], v[224:227], v[26:29]
	v_mfma_i32_16x16x64_i8 v[18:21], v[200:203], v[224:227], v[18:21]
	v_mfma_i32_16x16x64_i8 v[10:13], v[192:195], v[232:235], v[10:13]
	v_mfma_i32_16x16x64_i8 v[2:5], v[200:203], v[232:235], v[2:5]
	v_mfma_i32_16x16x64_i8 v[58:61], v[196:199], v[212:215], v[58:61]
	v_mfma_i32_16x16x64_i8 v[50:53], v[204:207], v[212:215], v[50:53]
	v_mfma_i32_16x16x64_i8 v[42:45], v[196:199], v[220:223], v[42:45]
	v_mfma_i32_16x16x64_i8 v[34:37], v[204:207], v[220:223], v[34:37]
	v_mfma_i32_16x16x64_i8 v[26:29], v[196:199], v[228:231], v[26:29]
	v_mfma_i32_16x16x64_i8 v[18:21], v[204:207], v[228:231], v[18:21]
	v_mfma_i32_16x16x64_i8 v[10:13], v[196:199], v[236:239], v[10:13]
	v_mfma_i32_16x16x64_i8 v[2:5], v[204:207], v[236:239], v[2:5]
	s_setprio 0
	s_barrier
	s_add_i32 s31, s31, 2
	s_add_u32 s4, s4, 0x100
	s_addc_u32 s5, s5, 0
	s_cmp_gt_u32 s31, 13
	v_lshl_add_u64 v[94:95], v[94:95], 0, s[24:25]
	s_cbranch_scc0 .LBB0_2649
	s_and_b64 vcc, exec, s[22:23]
	s_cbranch_vccz .LBB0_2652
	s_barrier
.LBB0_2652:
	s_ashr_i32 s41, s40, 31
	s_lshl_b64 s[4:5], s[40:41], 2
	s_add_u32 s4, s33, s4
	s_addc_u32 s5, s48, s5
	v_mov_b32_e32 v96, s100
	v_readfirstlane_b32 s101, v255
	v_lshl_add_u32 v94, s40, 8, v154
	v_ashrrev_i32_e32 v95, 31, v94
	v_lshl_add_u64 v[188:189], v[94:95], 2, s[14:15]
	v_lshl_or_b32 v97, s38, 8, v156
	global_load_dword v184, v[188:189], off
	v_cvt_f32_i32_e32 v192, v122
	v_cvt_f32_i32_e32 v194, v118
	v_cvt_f32_i32_e32 v196, v114
	v_cvt_f32_i32_e32 v198, v120
	v_cvt_f32_i32_e32 v200, v116
	v_cvt_f32_i32_e32 v143, v143
	v_cvt_f32_i32_e32 v142, v142
	v_cvt_f32_i32_e32 v139, v139
	v_cvt_f32_i32_e32 v138, v138
	v_cvt_f32_i32_e32 v135, v135
	v_cvt_f32_i32_e32 v134, v134
	v_cvt_f32_i32_e32 v191, v131
	v_cvt_f32_i32_e32 v190, v130
	v_cvt_f32_i32_e32 v127, v127
	v_cvt_f32_i32_e32 v126, v126
	v_cvt_f32_i32_e32 v193, v123
	v_cvt_f32_i32_e32 v129, v129
	v_cvt_f32_i32_e32 v128, v128
	v_cvt_f32_i32_e32 v125, v125
	v_cvt_f32_i32_e32 v124, v124
	v_cvt_f32_i32_e32 v195, v119
	v_cvt_f32_i32_e32 v197, v115
	v_cvt_f32_i32_e32 v145, v145
	v_cvt_f32_i32_e32 v144, v144
	v_cvt_f32_i32_e32 v141, v141
	v_cvt_f32_i32_e32 v140, v140
	v_cvt_f32_i32_e32 v137, v137
	v_cvt_f32_i32_e32 v136, v136
	v_cvt_f32_i32_e32 v133, v133
	v_cvt_f32_i32_e32 v132, v132
	v_cvt_f32_i32_e32 v199, v121
	v_cvt_f32_i32_e32 v201, v117
	v_mov_b32_e32 v130, 0
	v_mov_b32_e32 v131, 0
	v_mov_b32_e32 v202, 0
	v_mov_b32_e32 v203, 0
	v_cvt_f32_i32_e32 v103, v103
	v_cvt_f32_i32_e32 v102, v102
	s_mul_i32 s4, s40, 44
	s_add_i32 s4, s4, s38
	s_ashr_i32 s5, s4, 31
	v_cvt_f32_i32_e32 v91, v91
	v_cvt_f32_i32_e32 v90, v90
	s_lshl_b64 s[4:5], s[4:5], 15
	v_lshl_add_u64 v[206:207], v[160:161], 0, s[4:5]
	v_cvt_f32_i32_e32 v105, v105
	v_cvt_f32_i32_e32 v104, v104
	v_cvt_f32_i32_e32 v93, v93
	v_cvt_f32_i32_e32 v92, v92
	v_cvt_f32_i32_e32 v87, v87
	v_cvt_f32_i32_e32 v86, v86
	v_cvt_f32_i32_e32 v89, v89
	v_cvt_f32_i32_e32 v88, v88
	v_cvt_f32_i32_e32 v83, v83
	v_cvt_f32_i32_e32 v82, v82
	v_cvt_f32_i32_e32 v85, v85
	v_cvt_f32_i32_e32 v84, v84
	v_cvt_f32_i32_e32 v79, v79
	v_cvt_f32_i32_e32 v78, v78
	v_cvt_f32_i32_e32 v75, v75
	v_cvt_f32_i32_e32 v74, v74
	v_cvt_f32_i32_e32 v81, v81
	v_cvt_f32_i32_e32 v80, v80
	v_cvt_f32_i32_e32 v77, v77
	v_cvt_f32_i32_e32 v76, v76
	v_cvt_f32_i32_e32 v71, v71
	v_cvt_f32_i32_e32 v70, v70
	v_cvt_f32_i32_e32 v73, v73
	v_cvt_f32_i32_e32 v72, v72
	v_cvt_f32_i32_e32 v67, v67
	v_cvt_f32_i32_e32 v66, v66
	v_cvt_f32_i32_e32 v69, v69
	v_cvt_f32_i32_e32 v68, v68
	v_cvt_f32_i32_e32 v63, v63
	v_mul_lo_u32 v94, v96, s64
	v_add_u32_e32 v94, v97, v94
	v_ashrrev_i32_e32 v95, 31, v94
	v_lshl_add_u64 v[94:95], v[94:95], 2, s[16:17]
	global_load_dwordx4 v[110:113], v[94:95], off
	global_load_dwordx4 v[106:109], v[94:95], off offset:512
	global_load_dwordx4 v[98:101], v[94:95], off offset:16
	s_nop 0
	global_load_dwordx4 v[94:97], v[94:95], off offset:528
	s_nop 0
	global_load_dword v186, v[188:189], off offset:64
	global_load_dword v204, v[188:189], off offset:128
	global_load_dword v122, v[188:189], off offset:192
	global_load_dword v120, v[188:189], off offset:512
	global_load_dword v118, v[188:189], off offset:576
	global_load_dword v116, v[188:189], off offset:640
	global_load_dword v114, v[188:189], off offset:704
	v_lshl_add_u64 v[188:189], v[158:159], 0, s[4:5]
	v_cvt_f32_i32_e32 v62, v62
	v_cvt_f32_i32_e32 v59, v59
	v_cvt_f32_i32_e32 v58, v58
	v_cvt_f32_i32_e32 v65, v65
	v_cvt_f32_i32_e32 v64, v64
	v_cvt_f32_i32_e32 v61, v61
	v_cvt_f32_i32_e32 v60, v60
	v_cvt_f32_i32_e32 v55, v55
	v_cvt_f32_i32_e32 v54, v54
	v_cvt_f32_i32_e32 v57, v57
	v_cvt_f32_i32_e32 v56, v56
	v_cvt_f32_i32_e32 v51, v51
	v_cvt_f32_i32_e32 v50, v50
	v_cvt_f32_i32_e32 v53, v53
	v_cvt_f32_i32_e32 v52, v52
	v_cvt_f32_i32_e32 v47, v47
	v_cvt_f32_i32_e32 v46, v46
	v_cvt_f32_i32_e32 v43, v43
	v_cvt_f32_i32_e32 v42, v42
	v_cvt_f32_i32_e32 v49, v49
	v_cvt_f32_i32_e32 v48, v48
	v_cvt_f32_i32_e32 v45, v45
	v_cvt_f32_i32_e32 v44, v44
	v_cvt_f32_i32_e32 v39, v39
	v_cvt_f32_i32_e32 v38, v38
	v_cvt_f32_i32_e32 v41, v41
	v_cvt_f32_i32_e32 v40, v40
	v_cvt_f32_i32_e32 v35, v35
	v_cvt_f32_i32_e32 v34, v34
	v_cvt_f32_i32_e32 v37, v37
	v_cvt_f32_i32_e32 v36, v36
	v_cvt_f32_i32_e32 v31, v31
	v_cvt_f32_i32_e32 v30, v30
	v_cvt_f32_i32_e32 v27, v27
	v_cvt_f32_i32_e32 v26, v26
	v_cvt_f32_i32_e32 v33, v33
	v_cvt_f32_i32_e32 v32, v32
	v_cvt_f32_i32_e32 v29, v29
	v_cvt_f32_i32_e32 v28, v28
	v_cvt_f32_i32_e32 v23, v23
	v_cvt_f32_i32_e32 v22, v22
	v_cvt_f32_i32_e32 v25, v25
	v_cvt_f32_i32_e32 v24, v24
	v_cvt_f32_i32_e32 v19, v19
	v_cvt_f32_i32_e32 v18, v18
	v_cvt_f32_i32_e32 v21, v21
	v_cvt_f32_i32_e32 v20, v20
	v_cvt_f32_i32_e32 v15, v15
	v_cvt_f32_i32_e32 v14, v14
	v_cvt_f32_i32_e32 v11, v11
	v_cvt_f32_i32_e32 v10, v10
	v_cvt_f32_i32_e32 v17, v17
	v_cvt_f32_i32_e32 v16, v16
	v_cvt_f32_i32_e32 v13, v13
	v_cvt_f32_i32_e32 v12, v12
	v_cvt_f32_i32_e32 v7, v7
	v_cvt_f32_i32_e32 v6, v6
	v_cvt_f32_i32_e32 v9, v9
	v_cvt_f32_i32_e32 v8, v8
	v_cvt_f32_i32_e32 v3, v3
	v_cvt_f32_i32_e32 v2, v2
	v_cvt_f32_i32_e32 v5, v5
	v_cvt_f32_i32_e32 v4, v4
	s_and_b64 vcc, exec, s[0:1]
	s_mov_b64 s[0:1], -1
	s_waitcnt vmcnt(10)
	v_pk_mul_f32 v[210:211], v[110:111], v[184:185] op_sel_hi:[1,0]
	s_waitcnt vmcnt(9)
	v_pk_mul_f32 v[214:215], v[106:107], v[184:185] op_sel_hi:[1,0]
	s_waitcnt vmcnt(8)
	v_pk_mul_f32 v[218:219], v[98:99], v[184:185] op_sel_hi:[1,0]
	s_waitcnt vmcnt(7)
	v_pk_mul_f32 v[222:223], v[94:95], v[184:185] op_sel_hi:[1,0]
	s_waitcnt vmcnt(6)
	v_pk_mul_f32 v[224:225], v[112:113], v[186:187] op_sel_hi:[1,0]
	v_pk_mul_f32 v[226:227], v[110:111], v[186:187] op_sel_hi:[1,0]
	v_pk_mul_f32 v[228:229], v[108:109], v[186:187] op_sel_hi:[1,0]
	v_pk_mul_f32 v[230:231], v[106:107], v[186:187] op_sel_hi:[1,0]
	v_pk_mul_f32 v[234:235], v[98:99], v[186:187] op_sel_hi:[1,0]
	v_pk_mul_f32 v[238:239], v[94:95], v[186:187] op_sel_hi:[1,0]
	v_pk_mul_f32 v[142:143], v[210:211], v[142:143]
	v_pk_mul_f32 v[138:139], v[214:215], v[138:139]
	v_pk_mul_f32 v[134:135], v[218:219], v[134:135]
	v_pk_mul_f32 v[190:191], v[222:223], v[190:191]
	v_pk_mul_f32 v[126:127], v[226:227], v[126:127]
	v_pk_mul_f32 v[192:193], v[230:231], v[192:193]
	v_pk_mul_f32 v[128:129], v[224:225], v[128:129]
	v_pk_mul_f32 v[124:125], v[228:229], v[124:125]
	v_pk_mul_f32 v[194:195], v[234:235], v[194:195]
	v_pk_mul_f32 v[196:197], v[238:239], v[196:197]
	v_pk_mul_f32 v[138:139], v[142:143], v[138:139]
	v_pk_mul_f32 v[142:143], v[142:143], s[26:27] op_sel_hi:[1,0]
	v_pk_mul_f32 v[190:191], v[134:135], v[190:191]
	v_pk_mul_f32 v[134:135], v[134:135], s[26:27] op_sel_hi:[1,0]
	v_pk_mul_f32 v[192:193], v[126:127], v[192:193]
	v_pk_mul_f32 v[126:127], v[126:127], s[26:27] op_sel_hi:[1,0]
	v_pk_mul_f32 v[124:125], v[128:129], v[124:125]
	v_pk_mul_f32 v[128:129], v[128:129], s[26:27] op_sel_hi:[1,0]
	v_pk_mul_f32 v[196:197], v[194:195], v[196:197]
	v_pk_mul_f32 v[194:195], v[194:195], s[26:27] op_sel_hi:[1,0]
	v_exp_f32_e32 v142, v142
	v_exp_f32_e32 v143, v143
	v_exp_f32_e32 v134, v134
	v_exp_f32_e32 v135, v135
	v_pk_mul_f32 v[208:209], v[112:113], v[184:185] op_sel_hi:[1,0]
	v_pk_mul_f32 v[212:213], v[108:109], v[184:185] op_sel_hi:[1,0]
	v_pk_mul_f32 v[216:217], v[100:101], v[184:185] op_sel_hi:[1,0]
	v_pk_mul_f32 v[220:221], v[96:97], v[184:185] op_sel_hi:[1,0]
	v_exp_f32_e32 v126, v126
	v_exp_f32_e32 v127, v127
	v_exp_f32_e32 v128, v128
	v_exp_f32_e32 v129, v129
	v_exp_f32_e32 v194, v194
	v_exp_f32_e32 v195, v195
	v_pk_mul_f32 v[232:233], v[100:101], v[186:187] op_sel_hi:[1,0]
	v_pk_mul_f32 v[236:237], v[96:97], v[186:187] op_sel_hi:[1,0]
	v_pk_mul_f32 v[144:145], v[208:209], v[144:145]
	v_pk_mul_f32 v[140:141], v[212:213], v[140:141]
	v_pk_mul_f32 v[136:137], v[216:217], v[136:137]
	v_pk_mul_f32 v[132:133], v[220:221], v[132:133]
	v_pk_mul_f32 v[198:199], v[232:233], v[198:199]
	v_pk_mul_f32 v[200:201], v[236:237], v[200:201]
	v_pk_mul_f32 v[140:141], v[144:145], v[140:141]
	v_pk_mul_f32 v[144:145], v[144:145], s[26:27] op_sel_hi:[1,0]
	v_pk_mul_f32 v[132:133], v[136:137], v[132:133]
	v_pk_mul_f32 v[136:137], v[136:137], s[26:27] op_sel_hi:[1,0]
	v_pk_mul_f32 v[200:201], v[198:199], v[200:201]
	v_pk_mul_f32 v[198:199], v[198:199], s[26:27] op_sel_hi:[1,0]
	v_exp_f32_e32 v144, v144
	v_exp_f32_e32 v145, v145
	v_exp_f32_e32 v136, v136
	v_exp_f32_e32 v137, v137
	v_pk_add_f32 v[142:143], v[142:143], 1.0 op_sel_hi:[1,0]
	v_pk_add_f32 v[134:135], v[134:135], 1.0 op_sel_hi:[1,0]
	v_exp_f32_e32 v198, v198
	v_exp_f32_e32 v199, v199
	v_pk_add_f32 v[126:127], v[126:127], 1.0 op_sel_hi:[1,0]
	v_pk_add_f32 v[128:129], v[128:129], 1.0 op_sel_hi:[1,0]
	v_pk_add_f32 v[194:195], v[194:195], 1.0 op_sel_hi:[1,0]
	v_rcp_f32_e32 v142, v142
	v_rcp_f32_e32 v143, v143
	v_rcp_f32_e32 v134, v134
	v_rcp_f32_e32 v135, v135
	v_rcp_f32_e32 v126, v126
	v_rcp_f32_e32 v127, v127
	v_rcp_f32_e32 v128, v128
	v_rcp_f32_e32 v129, v129
	v_rcp_f32_e32 v194, v194
	v_rcp_f32_e32 v195, v195
	v_pk_add_f32 v[144:145], v[144:145], 1.0 op_sel_hi:[1,0]
	v_pk_add_f32 v[136:137], v[136:137], 1.0 op_sel_hi:[1,0]
	v_pk_add_f32 v[198:199], v[198:199], 1.0 op_sel_hi:[1,0]
	v_rcp_f32_e32 v144, v144
	v_rcp_f32_e32 v145, v145
	v_rcp_f32_e32 v136, v136
	v_rcp_f32_e32 v137, v137
	v_pk_mul_f32 v[138:139], v[138:139], v[142:143]
	v_pk_mul_f32 v[134:135], v[190:191], v[134:135]
	v_rcp_f32_e32 v198, v198
	v_rcp_f32_e32 v199, v199
	v_pk_mul_f32 v[126:127], v[192:193], v[126:127]
	v_pk_mul_f32 v[124:125], v[124:125], v[128:129]
	v_pk_mul_f32 v[128:129], v[196:197], v[194:195]
	v_med3_f32 v115, v138, s65, v187
	v_med3_f32 v117, v139, s65, v187
	v_med3_f32 v123, v134, s65, v187
	v_med3_f32 v134, v135, s65, v187
	v_med3_f32 v126, v126, s65, v187
	v_med3_f32 v127, v127, s65, v187
	v_med3_f32 v128, v128, s65, v187
	v_med3_f32 v129, v129, s65, v187
	v_cvt_pk_fp8_f32 v130, v115, v117
	v_cvt_pk_fp8_f32 v131, v123, v134
	v_cvt_pk_fp8_f32 v202, v126, v127
	v_cvt_pk_fp8_f32 v203, v128, v129
	v_pk_mul_f32 v[140:141], v[140:141], v[144:145]
	v_pk_mul_f32 v[132:133], v[132:133], v[136:137]
	v_pk_mul_f32 v[136:137], v[200:201], v[198:199]
	v_med3_f32 v119, v140, s65, v187
	v_med3_f32 v121, v141, s65, v187
	v_med3_f32 v132, v132, s65, v187
	v_med3_f32 v133, v133, s65, v187
	s_waitcnt vmcnt(5)
	v_pk_mul_f32 v[126:127], v[110:111], v[204:205] op_sel_hi:[1,0]
	v_med3_f32 v124, v124, s65, v187
	v_med3_f32 v125, v125, s65, v187
	v_med3_f32 v135, v136, s65, v187
	v_med3_f32 v136, v137, s65, v187
	v_cvt_pk_fp8_f32 v130, v119, v121 op_sel:[0,0,1]
	v_cvt_pk_fp8_f32 v131, v132, v133 op_sel:[0,0,1]
	v_pk_mul_f32 v[102:103], v[126:127], v[102:103]
	v_cvt_pk_fp8_f32 v202, v124, v125 op_sel:[0,0,1]
	v_cvt_pk_fp8_f32 v203, v135, v136 op_sel:[0,0,1]
	v_pk_mul_f32 v[126:127], v[102:103], s[26:27] op_sel_hi:[1,0]
	global_store_dwordx2 v[188:189], v[130:131], off
	global_store_dwordx2 v[206:207], v[202:203], off
	v_exp_f32_e32 v126, v126
	v_exp_f32_e32 v127, v127
	v_pk_mul_f32 v[130:131], v[106:107], v[204:205] op_sel_hi:[1,0]
	v_pk_mul_f32 v[124:125], v[112:113], v[204:205] op_sel_hi:[1,0]
	v_pk_mul_f32 v[90:91], v[130:131], v[90:91]
	v_pk_mul_f32 v[128:129], v[108:109], v[204:205] op_sel_hi:[1,0]
	v_pk_mul_f32 v[90:91], v[102:103], v[90:91]
	v_pk_add_f32 v[102:103], v[126:127], 1.0 op_sel_hi:[1,0]
	v_pk_mul_f32 v[104:105], v[124:125], v[104:105]
	v_rcp_f32_e32 v102, v102
	v_rcp_f32_e32 v103, v103
	v_pk_mul_f32 v[92:93], v[128:129], v[92:93]
	v_pk_mul_f32 v[124:125], v[104:105], s[26:27] op_sel_hi:[1,0]
	v_pk_mul_f32 v[92:93], v[104:105], v[92:93]
	v_pk_mul_f32 v[104:105], v[98:99], v[204:205] op_sel_hi:[1,0]
	v_exp_f32_e32 v124, v124
	v_exp_f32_e32 v125, v125
	v_pk_mul_f32 v[90:91], v[90:91], v[102:103]
	v_pk_mul_f32 v[102:103], v[100:101], v[204:205] op_sel_hi:[1,0]
	v_pk_mul_f32 v[86:87], v[104:105], v[86:87]
	v_pk_mul_f32 v[88:89], v[102:103], v[88:89]
	v_pk_mul_f32 v[104:105], v[86:87], s[26:27] op_sel_hi:[1,0]
	v_pk_mul_f32 v[102:103], v[88:89], s[26:27] op_sel_hi:[1,0]
	v_exp_f32_e32 v104, v104
	v_exp_f32_e32 v105, v105
	v_exp_f32_e32 v102, v102
	v_exp_f32_e32 v103, v103
	v_pk_add_f32 v[124:125], v[124:125], 1.0 op_sel_hi:[1,0]
	v_pk_mul_f32 v[126:127], v[94:95], v[204:205] op_sel_hi:[1,0]
	v_rcp_f32_e32 v124, v124
	v_rcp_f32_e32 v125, v125
	v_pk_mul_f32 v[82:83], v[126:127], v[82:83]
	v_pk_add_f32 v[102:103], v[102:103], 1.0 op_sel_hi:[1,0]
	v_pk_mul_f32 v[82:83], v[86:87], v[82:83]
	v_pk_add_f32 v[86:87], v[104:105], 1.0 op_sel_hi:[1,0]
	v_rcp_f32_e32 v102, v102
	v_rcp_f32_e32 v86, v86
	v_rcp_f32_e32 v87, v87
	v_rcp_f32_e32 v103, v103
	v_pk_mul_f32 v[92:93], v[92:93], v[124:125]
	v_pk_mul_f32 v[124:125], v[96:97], v[204:205] op_sel_hi:[1,0]
	v_pk_mul_f32 v[82:83], v[82:83], v[86:87]
	v_pk_mul_f32 v[84:85], v[124:125], v[84:85]
	v_med3_f32 v87, v90, s65, v187
	v_pk_mul_f32 v[84:85], v[88:89], v[84:85]
	v_med3_f32 v88, v91, s65, v187
	v_mov_b32_e32 v86, 0
	v_pk_mul_f32 v[84:85], v[84:85], v[102:103]
	v_cvt_pk_fp8_f32 v86, v87, v88
	v_med3_f32 v82, v82, s65, v187
	v_med3_f32 v83, v83, s65, v187
	v_mov_b32_e32 v87, 0
	v_cvt_pk_fp8_f32 v87, v82, v83
	v_med3_f32 v82, v84, s65, v187
	v_med3_f32 v83, v85, s65, v187
	s_waitcnt vmcnt(6)
	v_pk_mul_f32 v[84:85], v[110:111], v[122:123] op_sel_hi:[1,0]
	v_med3_f32 v89, v92, s65, v187
	v_pk_mul_f32 v[78:79], v[84:85], v[78:79]
	v_med3_f32 v90, v93, s65, v187
	v_pk_mul_f32 v[84:85], v[78:79], s[26:27] op_sel_hi:[1,0]
	v_cvt_pk_fp8_f32 v86, v89, v90 op_sel:[0,0,1]
	v_exp_f32_e32 v84, v84
	v_exp_f32_e32 v85, v85
	v_pk_mul_f32 v[90:91], v[106:107], v[122:123] op_sel_hi:[1,0]
	v_cvt_pk_fp8_f32 v87, v82, v83 op_sel:[0,0,1]
	v_pk_mul_f32 v[74:75], v[90:91], v[74:75]
	v_pk_mul_f32 v[82:83], v[112:113], v[122:123] op_sel_hi:[1,0]
	v_pk_mul_f32 v[74:75], v[78:79], v[74:75]
	v_pk_add_f32 v[78:79], v[84:85], 1.0 op_sel_hi:[1,0]
	v_pk_mul_f32 v[88:89], v[108:109], v[122:123] op_sel_hi:[1,0]
	v_rcp_f32_e32 v78, v78
	v_rcp_f32_e32 v79, v79
	v_pk_mul_f32 v[80:81], v[82:83], v[80:81]
	v_pk_mul_f32 v[76:77], v[88:89], v[76:77]
	v_pk_mul_f32 v[82:83], v[80:81], s[26:27] op_sel_hi:[1,0]
	v_pk_mul_f32 v[76:77], v[80:81], v[76:77]
	v_pk_mul_f32 v[80:81], v[98:99], v[122:123] op_sel_hi:[1,0]
	v_exp_f32_e32 v82, v82
	v_exp_f32_e32 v83, v83
	v_pk_mul_f32 v[74:75], v[74:75], v[78:79]
	v_pk_mul_f32 v[78:79], v[100:101], v[122:123] op_sel_hi:[1,0]
	v_pk_mul_f32 v[70:71], v[80:81], v[70:71]
	v_pk_mul_f32 v[72:73], v[78:79], v[72:73]
	v_pk_mul_f32 v[80:81], v[70:71], s[26:27] op_sel_hi:[1,0]
	v_pk_mul_f32 v[78:79], v[72:73], s[26:27] op_sel_hi:[1,0]
	v_exp_f32_e32 v80, v80
	v_exp_f32_e32 v81, v81
	v_exp_f32_e32 v78, v78
	v_exp_f32_e32 v79, v79
	v_pk_add_f32 v[82:83], v[82:83], 1.0 op_sel_hi:[1,0]
	v_pk_mul_f32 v[84:85], v[94:95], v[122:123] op_sel_hi:[1,0]
	v_rcp_f32_e32 v82, v82
	v_rcp_f32_e32 v83, v83
	v_pk_mul_f32 v[66:67], v[84:85], v[66:67]
	v_pk_add_f32 v[78:79], v[78:79], 1.0 op_sel_hi:[1,0]
	v_pk_mul_f32 v[66:67], v[70:71], v[66:67]
	v_pk_add_f32 v[70:71], v[80:81], 1.0 op_sel_hi:[1,0]
	v_rcp_f32_e32 v78, v78
	v_rcp_f32_e32 v70, v70
	v_rcp_f32_e32 v71, v71
	v_rcp_f32_e32 v79, v79
	v_pk_mul_f32 v[76:77], v[76:77], v[82:83]
	v_pk_mul_f32 v[82:83], v[96:97], v[122:123] op_sel_hi:[1,0]
	v_pk_mul_f32 v[66:67], v[66:67], v[70:71]
	v_pk_mul_f32 v[68:69], v[82:83], v[68:69]
	v_med3_f32 v71, v74, s65, v187
	v_pk_mul_f32 v[68:69], v[72:73], v[68:69]
	v_med3_f32 v72, v75, s65, v187
	v_mov_b32_e32 v70, 0
	v_pk_mul_f32 v[68:69], v[68:69], v[78:79]
	v_cvt_pk_fp8_f32 v70, v71, v72
	v_med3_f32 v66, v66, s65, v187
	v_med3_f32 v67, v67, s65, v187
	v_mov_b32_e32 v71, 0
	v_cvt_pk_fp8_f32 v71, v66, v67
	v_med3_f32 v66, v68, s65, v187
	v_med3_f32 v67, v69, s65, v187
	s_waitcnt vmcnt(5)
	v_pk_mul_f32 v[68:69], v[110:111], v[120:121] op_sel_hi:[1,0]
	v_med3_f32 v73, v76, s65, v187
	v_pk_mul_f32 v[62:63], v[68:69], v[62:63]
	v_med3_f32 v74, v77, s65, v187
	v_pk_mul_f32 v[68:69], v[62:63], s[26:27] op_sel_hi:[1,0]
	v_cvt_pk_fp8_f32 v70, v73, v74 op_sel:[0,0,1]
	v_exp_f32_e32 v68, v68
	v_exp_f32_e32 v69, v69
	v_cvt_pk_fp8_f32 v71, v66, v67 op_sel:[0,0,1]
	v_pk_mul_f32 v[72:73], v[106:107], v[120:121] op_sel_hi:[1,0]
	v_lshl_add_u64 v[66:67], v[164:165], 0, s[4:5]
	v_pk_mul_f32 v[58:59], v[72:73], v[58:59]
	global_store_dwordx2 v[66:67], v[86:87], off
	v_pk_mul_f32 v[58:59], v[62:63], v[58:59]
	v_pk_add_f32 v[62:63], v[68:69], 1.0 op_sel_hi:[1,0]
	v_lshl_add_u64 v[66:67], v[166:167], 0, s[4:5]
	v_rcp_f32_e32 v62, v62
	v_rcp_f32_e32 v63, v63
	global_store_dwordx2 v[66:67], v[70:71], off
	v_pk_mul_f32 v[66:67], v[112:113], v[120:121] op_sel_hi:[1,0]
	v_pk_mul_f32 v[70:71], v[108:109], v[120:121] op_sel_hi:[1,0]
	v_pk_mul_f32 v[64:65], v[66:67], v[64:65]
	v_pk_mul_f32 v[60:61], v[70:71], v[60:61]
	v_pk_mul_f32 v[66:67], v[64:65], s[26:27] op_sel_hi:[1,0]
	v_pk_mul_f32 v[60:61], v[64:65], v[60:61]
	v_pk_mul_f32 v[64:65], v[98:99], v[120:121] op_sel_hi:[1,0]
	v_exp_f32_e32 v66, v66
	v_exp_f32_e32 v67, v67
	v_pk_mul_f32 v[58:59], v[58:59], v[62:63]
	v_pk_mul_f32 v[62:63], v[100:101], v[120:121] op_sel_hi:[1,0]
	v_pk_mul_f32 v[54:55], v[64:65], v[54:55]
	v_pk_mul_f32 v[56:57], v[62:63], v[56:57]
	v_pk_mul_f32 v[64:65], v[54:55], s[26:27] op_sel_hi:[1,0]
	v_pk_mul_f32 v[62:63], v[56:57], s[26:27] op_sel_hi:[1,0]
	v_exp_f32_e32 v64, v64
	v_exp_f32_e32 v65, v65
	v_exp_f32_e32 v62, v62
	v_exp_f32_e32 v63, v63
	v_pk_add_f32 v[66:67], v[66:67], 1.0 op_sel_hi:[1,0]
	v_pk_mul_f32 v[68:69], v[94:95], v[120:121] op_sel_hi:[1,0]
	v_rcp_f32_e32 v66, v66
	v_rcp_f32_e32 v67, v67
	v_pk_mul_f32 v[50:51], v[68:69], v[50:51]
	v_pk_add_f32 v[62:63], v[62:63], 1.0 op_sel_hi:[1,0]
	v_pk_mul_f32 v[50:51], v[54:55], v[50:51]
	v_pk_add_f32 v[54:55], v[64:65], 1.0 op_sel_hi:[1,0]
	v_rcp_f32_e32 v62, v62
	v_rcp_f32_e32 v54, v54
	v_rcp_f32_e32 v55, v55
	v_rcp_f32_e32 v63, v63
	v_pk_mul_f32 v[60:61], v[60:61], v[66:67]
	v_pk_mul_f32 v[66:67], v[96:97], v[120:121] op_sel_hi:[1,0]
	v_pk_mul_f32 v[50:51], v[50:51], v[54:55]
	v_pk_mul_f32 v[52:53], v[66:67], v[52:53]
	v_med3_f32 v55, v58, s65, v187
	v_pk_mul_f32 v[52:53], v[56:57], v[52:53]
	v_med3_f32 v56, v59, s65, v187
	v_mov_b32_e32 v54, 0
	v_pk_mul_f32 v[52:53], v[52:53], v[62:63]
	v_cvt_pk_fp8_f32 v54, v55, v56
	v_med3_f32 v50, v50, s65, v187
	v_med3_f32 v51, v51, s65, v187
	v_mov_b32_e32 v55, 0
	v_cvt_pk_fp8_f32 v55, v50, v51
	v_med3_f32 v50, v52, s65, v187
	v_med3_f32 v51, v53, s65, v187
	s_waitcnt vmcnt(6)
	v_pk_mul_f32 v[52:53], v[110:111], v[118:119] op_sel_hi:[1,0]
	v_med3_f32 v57, v60, s65, v187
	v_pk_mul_f32 v[46:47], v[52:53], v[46:47]
	v_med3_f32 v58, v61, s65, v187
	v_pk_mul_f32 v[52:53], v[46:47], s[26:27] op_sel_hi:[1,0]
	v_cvt_pk_fp8_f32 v54, v57, v58 op_sel:[0,0,1]
	v_exp_f32_e32 v52, v52
	v_exp_f32_e32 v53, v53
	v_pk_mul_f32 v[58:59], v[106:107], v[118:119] op_sel_hi:[1,0]
	v_cvt_pk_fp8_f32 v55, v50, v51 op_sel:[0,0,1]
	v_pk_mul_f32 v[42:43], v[58:59], v[42:43]
	v_pk_mul_f32 v[50:51], v[112:113], v[118:119] op_sel_hi:[1,0]
	v_pk_mul_f32 v[42:43], v[46:47], v[42:43]
	v_pk_add_f32 v[46:47], v[52:53], 1.0 op_sel_hi:[1,0]
	v_pk_mul_f32 v[56:57], v[108:109], v[118:119] op_sel_hi:[1,0]
	v_rcp_f32_e32 v46, v46
	v_rcp_f32_e32 v47, v47
	v_pk_mul_f32 v[48:49], v[50:51], v[48:49]
	v_pk_mul_f32 v[44:45], v[56:57], v[44:45]
	v_pk_mul_f32 v[50:51], v[48:49], s[26:27] op_sel_hi:[1,0]
	v_pk_mul_f32 v[44:45], v[48:49], v[44:45]
	v_pk_mul_f32 v[48:49], v[98:99], v[118:119] op_sel_hi:[1,0]
	v_exp_f32_e32 v50, v50
	v_exp_f32_e32 v51, v51
	v_pk_mul_f32 v[42:43], v[42:43], v[46:47]
	v_pk_mul_f32 v[46:47], v[100:101], v[118:119] op_sel_hi:[1,0]
	v_pk_mul_f32 v[38:39], v[48:49], v[38:39]
	v_pk_mul_f32 v[40:41], v[46:47], v[40:41]
	v_pk_mul_f32 v[48:49], v[38:39], s[26:27] op_sel_hi:[1,0]
	v_pk_mul_f32 v[46:47], v[40:41], s[26:27] op_sel_hi:[1,0]
	v_exp_f32_e32 v48, v48
	v_exp_f32_e32 v49, v49
	v_exp_f32_e32 v46, v46
	v_exp_f32_e32 v47, v47
	v_pk_add_f32 v[50:51], v[50:51], 1.0 op_sel_hi:[1,0]
	v_pk_mul_f32 v[52:53], v[94:95], v[118:119] op_sel_hi:[1,0]
	v_rcp_f32_e32 v50, v50
	v_rcp_f32_e32 v51, v51
	v_pk_mul_f32 v[34:35], v[52:53], v[34:35]
	v_pk_add_f32 v[46:47], v[46:47], 1.0 op_sel_hi:[1,0]
	v_pk_mul_f32 v[34:35], v[38:39], v[34:35]
	v_pk_add_f32 v[38:39], v[48:49], 1.0 op_sel_hi:[1,0]
	v_rcp_f32_e32 v46, v46
	v_rcp_f32_e32 v38, v38
	v_rcp_f32_e32 v39, v39
	v_rcp_f32_e32 v47, v47
	v_pk_mul_f32 v[44:45], v[44:45], v[50:51]
	v_pk_mul_f32 v[50:51], v[96:97], v[118:119] op_sel_hi:[1,0]
	v_pk_mul_f32 v[34:35], v[34:35], v[38:39]
	v_pk_mul_f32 v[36:37], v[50:51], v[36:37]
	v_med3_f32 v39, v42, s65, v187
	v_pk_mul_f32 v[36:37], v[40:41], v[36:37]
	v_med3_f32 v40, v43, s65, v187
	v_mov_b32_e32 v38, 0
	v_pk_mul_f32 v[36:37], v[36:37], v[46:47]
	v_cvt_pk_fp8_f32 v38, v39, v40
	v_med3_f32 v34, v34, s65, v187
	v_med3_f32 v35, v35, s65, v187
	v_mov_b32_e32 v39, 0
	v_cvt_pk_fp8_f32 v39, v34, v35
	v_med3_f32 v34, v36, s65, v187
	v_med3_f32 v35, v37, s65, v187
	s_waitcnt vmcnt(5)
	v_pk_mul_f32 v[36:37], v[110:111], v[116:117] op_sel_hi:[1,0]
	v_med3_f32 v41, v44, s65, v187
	v_pk_mul_f32 v[30:31], v[36:37], v[30:31]
	v_med3_f32 v42, v45, s65, v187
	v_pk_mul_f32 v[36:37], v[30:31], s[26:27] op_sel_hi:[1,0]
	v_cvt_pk_fp8_f32 v38, v41, v42 op_sel:[0,0,1]
	v_exp_f32_e32 v36, v36
	v_exp_f32_e32 v37, v37
	v_cvt_pk_fp8_f32 v39, v34, v35 op_sel:[0,0,1]
	v_pk_mul_f32 v[40:41], v[106:107], v[116:117] op_sel_hi:[1,0]
	v_lshl_add_u64 v[34:35], v[168:169], 0, s[4:5]
	v_pk_mul_f32 v[26:27], v[40:41], v[26:27]
	global_store_dwordx2 v[34:35], v[54:55], off
	v_pk_mul_f32 v[26:27], v[30:31], v[26:27]
	v_pk_add_f32 v[30:31], v[36:37], 1.0 op_sel_hi:[1,0]
	v_lshl_add_u64 v[34:35], v[170:171], 0, s[4:5]
	v_rcp_f32_e32 v30, v30
	v_rcp_f32_e32 v31, v31
	global_store_dwordx2 v[34:35], v[38:39], off
	v_pk_mul_f32 v[34:35], v[112:113], v[116:117] op_sel_hi:[1,0]
	v_pk_mul_f32 v[38:39], v[108:109], v[116:117] op_sel_hi:[1,0]
	v_pk_mul_f32 v[32:33], v[34:35], v[32:33]
	v_pk_mul_f32 v[28:29], v[38:39], v[28:29]
	v_pk_mul_f32 v[34:35], v[32:33], s[26:27] op_sel_hi:[1,0]
	v_pk_mul_f32 v[28:29], v[32:33], v[28:29]
	v_pk_mul_f32 v[32:33], v[98:99], v[116:117] op_sel_hi:[1,0]
	v_exp_f32_e32 v34, v34
	v_exp_f32_e32 v35, v35
	v_pk_mul_f32 v[26:27], v[26:27], v[30:31]
	v_pk_mul_f32 v[30:31], v[100:101], v[116:117] op_sel_hi:[1,0]
	v_pk_mul_f32 v[22:23], v[32:33], v[22:23]
	v_pk_mul_f32 v[24:25], v[30:31], v[24:25]
	v_pk_mul_f32 v[32:33], v[22:23], s[26:27] op_sel_hi:[1,0]
	v_pk_mul_f32 v[30:31], v[24:25], s[26:27] op_sel_hi:[1,0]
	v_exp_f32_e32 v32, v32
	v_exp_f32_e32 v33, v33
	v_exp_f32_e32 v30, v30
	v_exp_f32_e32 v31, v31
	v_pk_add_f32 v[34:35], v[34:35], 1.0 op_sel_hi:[1,0]
	v_pk_mul_f32 v[36:37], v[94:95], v[116:117] op_sel_hi:[1,0]
	v_rcp_f32_e32 v34, v34
	v_rcp_f32_e32 v35, v35
	v_pk_mul_f32 v[18:19], v[36:37], v[18:19]
	v_pk_add_f32 v[30:31], v[30:31], 1.0 op_sel_hi:[1,0]
	v_pk_mul_f32 v[18:19], v[22:23], v[18:19]
	v_pk_add_f32 v[22:23], v[32:33], 1.0 op_sel_hi:[1,0]
	v_rcp_f32_e32 v30, v30
	v_rcp_f32_e32 v22, v22
	v_rcp_f32_e32 v23, v23
	v_rcp_f32_e32 v31, v31
	v_pk_mul_f32 v[28:29], v[28:29], v[34:35]
	v_pk_mul_f32 v[34:35], v[96:97], v[116:117] op_sel_hi:[1,0]
	v_pk_mul_f32 v[18:19], v[18:19], v[22:23]
	v_pk_mul_f32 v[20:21], v[34:35], v[20:21]
	v_med3_f32 v23, v26, s65, v187
	v_pk_mul_f32 v[20:21], v[24:25], v[20:21]
	v_med3_f32 v24, v27, s65, v187
	v_mov_b32_e32 v22, 0
	v_pk_mul_f32 v[20:21], v[20:21], v[30:31]
	v_cvt_pk_fp8_f32 v22, v23, v24
	v_med3_f32 v18, v18, s65, v187
	v_med3_f32 v19, v19, s65, v187
	v_mov_b32_e32 v23, 0
	v_cvt_pk_fp8_f32 v23, v18, v19
	v_med3_f32 v18, v20, s65, v187
	v_med3_f32 v19, v21, s65, v187
	s_waitcnt vmcnt(6)
	v_pk_mul_f32 v[20:21], v[110:111], v[114:115] op_sel_hi:[1,0]
	v_med3_f32 v25, v28, s65, v187
	v_pk_mul_f32 v[14:15], v[20:21], v[14:15]
	v_med3_f32 v26, v29, s65, v187
	v_pk_mul_f32 v[20:21], v[14:15], s[26:27] op_sel_hi:[1,0]
	v_cvt_pk_fp8_f32 v22, v25, v26 op_sel:[0,0,1]
	v_exp_f32_e32 v20, v20
	v_exp_f32_e32 v21, v21
	v_pk_mul_f32 v[26:27], v[106:107], v[114:115] op_sel_hi:[1,0]
	v_cvt_pk_fp8_f32 v23, v18, v19 op_sel:[0,0,1]
	v_pk_mul_f32 v[18:19], v[112:113], v[114:115] op_sel_hi:[1,0]
	v_pk_mul_f32 v[24:25], v[108:109], v[114:115] op_sel_hi:[1,0]
	v_pk_mul_f32 v[10:11], v[26:27], v[10:11]
	v_pk_mul_f32 v[16:17], v[18:19], v[16:17]
	v_pk_mul_f32 v[10:11], v[14:15], v[10:11]
	v_pk_add_f32 v[14:15], v[20:21], 1.0 op_sel_hi:[1,0]
	v_pk_mul_f32 v[12:13], v[24:25], v[12:13]
	v_rcp_f32_e32 v14, v14
	v_pk_mul_f32 v[18:19], v[16:17], s[26:27] op_sel_hi:[1,0]
	v_rcp_f32_e32 v15, v15
	v_pk_mul_f32 v[12:13], v[16:17], v[12:13]
	v_pk_mul_f32 v[16:17], v[98:99], v[114:115] op_sel_hi:[1,0]
	v_exp_f32_e32 v18, v18
	v_exp_f32_e32 v19, v19
	v_pk_mul_f32 v[6:7], v[16:17], v[6:7]
	v_pk_mul_f32 v[10:11], v[10:11], v[14:15]
	v_pk_mul_f32 v[16:17], v[6:7], s[26:27] op_sel_hi:[1,0]
	v_pk_mul_f32 v[14:15], v[100:101], v[114:115] op_sel_hi:[1,0]
	v_exp_f32_e32 v16, v16
	v_exp_f32_e32 v17, v17
	v_pk_add_f32 v[18:19], v[18:19], 1.0 op_sel_hi:[1,0]
	v_pk_mul_f32 v[20:21], v[94:95], v[114:115] op_sel_hi:[1,0]
	v_pk_mul_f32 v[8:9], v[14:15], v[8:9]
	v_rcp_f32_e32 v18, v18
	v_rcp_f32_e32 v19, v19
	v_pk_mul_f32 v[2:3], v[20:21], v[2:3]
	v_pk_mul_f32 v[14:15], v[8:9], s[26:27] op_sel_hi:[1,0]
	v_pk_mul_f32 v[2:3], v[6:7], v[2:3]
	v_pk_add_f32 v[6:7], v[16:17], 1.0 op_sel_hi:[1,0]
	v_exp_f32_e32 v14, v14
	v_exp_f32_e32 v15, v15
	v_rcp_f32_e32 v6, v6
	v_rcp_f32_e32 v7, v7
	v_pk_mul_f32 v[12:13], v[12:13], v[18:19]
	v_pk_mul_f32 v[18:19], v[96:97], v[114:115] op_sel_hi:[1,0]
	v_pk_add_f32 v[14:15], v[14:15], 1.0 op_sel_hi:[1,0]
	v_pk_mul_f32 v[4:5], v[18:19], v[4:5]
	v_rcp_f32_e32 v14, v14
	v_rcp_f32_e32 v15, v15
	v_pk_mul_f32 v[2:3], v[2:3], v[6:7]
	v_pk_mul_f32 v[4:5], v[8:9], v[4:5]
	v_med3_f32 v7, v10, s65, v187
	v_med3_f32 v8, v11, s65, v187
	v_mov_b32_e32 v6, 0
	v_cvt_pk_fp8_f32 v6, v7, v8
	v_med3_f32 v2, v2, s65, v187
	v_med3_f32 v3, v3, s65, v187
	v_mov_b32_e32 v7, 0
	v_cvt_pk_fp8_f32 v7, v2, v3
	v_pk_mul_f32 v[4:5], v[4:5], v[14:15]
	v_med3_f32 v9, v12, s65, v187
	v_med3_f32 v10, v13, s65, v187
	v_med3_f32 v2, v4, s65, v187
	v_med3_f32 v3, v5, s65, v187
	v_cvt_pk_fp8_f32 v6, v9, v10 op_sel:[0,0,1]
	v_cvt_pk_fp8_f32 v7, v2, v3 op_sel:[0,0,1]
	v_lshl_add_u64 v[2:3], v[172:173], 0, s[4:5]
	global_store_dwordx2 v[2:3], v[22:23], off
	v_lshl_add_u64 v[2:3], v[174:175], 0, s[4:5]
	global_store_dwordx2 v[2:3], v[6:7], off
	s_cbranch_vccnz .LBB0_2636
	s_andn2_b64 vcc, exec, s[12:13]
	s_cbranch_vccnz .LBB0_2635
	s_barrier
	s_branch .LBB0_2635

	.amdhsa_kernel _Z4mega4Args
		.amdhsa_group_segment_fixed_size 0
		.amdhsa_private_segment_fixed_size 0
		.amdhsa_kernarg_size 528
		.amdhsa_user_sgpr_count 2
		.amdhsa_user_sgpr_dispatch_ptr 0
		.amdhsa_user_sgpr_queue_ptr 0
		.amdhsa_user_sgpr_kernarg_segment_ptr 1
		.amdhsa_user_sgpr_dispatch_id 0
		.amdhsa_user_sgpr_kernarg_preload_length 0
		.amdhsa_user_sgpr_kernarg_preload_offset 0
		.amdhsa_user_sgpr_private_segment_size 0
		.amdhsa_uses_dynamic_stack 0
		.amdhsa_enable_private_segment 0
		.amdhsa_system_sgpr_workgroup_id_x 1
		.amdhsa_system_sgpr_workgroup_id_y 0
		.amdhsa_system_sgpr_workgroup_id_z 0
		.amdhsa_system_sgpr_workgroup_info 0
		.amdhsa_system_vgpr_workitem_id 0
		.amdhsa_next_free_vgpr 256
		.amdhsa_next_free_sgpr 102
		.amdhsa_accum_offset 256
		.amdhsa_reserve_vcc 1
		.amdhsa_float_round_mode_32 0
		.amdhsa_float_round_mode_16_64 0
		.amdhsa_float_denorm_mode_32 3
		.amdhsa_float_denorm_mode_16_64 3
		.amdhsa_dx10_clamp 1
		.amdhsa_ieee_mode 1
		.amdhsa_fp16_overflow 0
		.amdhsa_tg_split 0
		.amdhsa_exception_fp_ieee_invalid_op 0
		.amdhsa_exception_fp_denorm_src 0
		.amdhsa_exception_fp_ieee_div_zero 0
		.amdhsa_exception_fp_ieee_overflow 0
		.amdhsa_exception_fp_ieee_underflow 0
		.amdhsa_exception_fp_ieee_inexact 0
		.amdhsa_exception_int_div_zero 0
	.end_amdhsa_kernel

amdhsa.kernels:
  - .agpr_count:     0
    .args:
      - .offset:         0
        .size:           272
        .value_kind:     by_value
      - .offset:         272
        .size:           4
        .value_kind:     hidden_block_count_x
      - .offset:         276
        .size:           4
        .value_kind:     hidden_block_count_y
      - .offset:         280
        .size:           4
        .value_kind:     hidden_block_count_z
      - .offset:         284
        .size:           2
        .value_kind:     hidden_group_size_x
      - .offset:         286
        .size:           2
        .value_kind:     hidden_group_size_y
      - .offset:         288
        .size:           2
        .value_kind:     hidden_group_size_z
      - .offset:         290
        .size:           2
        .value_kind:     hidden_remainder_x
      - .offset:         292
        .size:           2
        .value_kind:     hidden_remainder_y
      - .offset:         294
        .size:           2
        .value_kind:     hidden_remainder_z
      - .offset:         312
        .size:           8
        .value_kind:     hidden_global_offset_x
      - .offset:         320
        .size:           8
        .value_kind:     hidden_global_offset_y
      - .offset:         328
        .size:           8
        .value_kind:     hidden_global_offset_z
      - .offset:         336
        .size:           2
        .value_kind:     hidden_grid_dims
      - .offset:         392
        .size:           4
        .value_kind:     hidden_dynamic_lds_size
    .group_segment_fixed_size: 0
    .kernarg_segment_align: 8
    .kernarg_segment_size: 528
    .language:       OpenCL C
    .language_version:
      - 2
      - 0
    .max_flat_workgroup_size: 512
    .name:           _Z4mega4Args
    .private_segment_fixed_size: 0
    .sgpr_count:     108
    .sgpr_spill_count: 71
    .symbol:         _Z4mega4Args.kd
    .uniform_work_group_size: 1
    .uses_dynamic_stack: false
    .vgpr_count:     256
    .vgpr_spill_count: 0
    .wavefront_size: 64
